# MoE hand-off: the readiness counter of the unit after next is read before the epilogue (wave 0), so the poll at the next unit boundary usually needs no load round trip
# baseline (speedup 1.0000x reference)
.LBB0_2030:
	v_readlane_b32 s24, v253, 60
	v_readlane_b32 s25, v253, 61
	s_lshl_b64 s[22:23], s[24:25], 18
	s_waitcnt lgkmcnt(0)
	s_add_u32 s72, s20, s22
	s_addc_u32 s73, s21, s23
	v_lshrrev_b32_e32 v11, 1, v18
	s_add_u32 s20, s2, 0x67734900
	v_and_b32_e32 v11, 24, v11
	s_addc_u32 s21, s3, 0
	s_lshl_b64 s[2:3], s[24:25], 17
	v_and_b32_e32 v10, 15, v18
	v_lshlrev_b32_e32 v12, 1, v11
	s_add_u32 s74, s6, s2
	v_lshl_or_b32 v157, s0, 6, v10
	v_lshl_or_b32 v10, v10, 6, v12
	v_lshlrev_b32_e32 v12, 2, v18
	s_addc_u32 s75, s7, s3
	s_lshl_b32 s0, s0, 13
	v_and_b32_e32 v12, 32, v12
	v_bitop3_b32 v13, v10, s0, v12 bitop3:0xde
	s_lshl_b32 s0, s1, 5
	s_and_b32 s2, s0, 0x60
	s_add_i32 m0, s68, 0x18000
	v_lshl_add_u64 v[8:9], v[8:9], 0, s[46:47]
	s_lshl_b32 s0, s2, 7
	s_waitcnt vmcnt(2)
	s_barrier
	global_load_lds_dwordx4 v[8:9], off
	v_lshl_add_u64 v[6:7], v[6:7], 0, s[46:47]
	s_add_i32 m0, s68, 0x1a000
	s_add_i32 s76, s68, 0x8000
	s_add_i32 s77, s68, 0xa000
	v_bitop3_b32 v159, s0, v10, v12 bitop3:0xf6
	global_load_lds_dwordx4 v[6:7], off
	v_lshl_add_u64 v[2:3], v[2:3], 0, s[46:47]
	s_mov_b32 m0, s76
	s_add_u32 s0, s52, 0x40080
	global_load_lds_dwordx4 v[2:3], off
	v_lshl_add_u64 v[2:3], v[4:5], 0, s[46:47]
	s_mov_b32 m0, s77
	s_addc_u32 s1, s53, 0
	global_load_lds_dwordx4 v[2:3], off
	s_add_i32 m0, s68, 0x1c000
	v_lshl_add_u64 v[2:3], s[0:1], 0, v[150:151]
	global_load_lds_dwordx4 v[2:3], off
	v_lshl_add_u64 v[2:3], s[0:1], 0, v[152:153]
	s_add_i32 m0, s68, 0x1e000
	s_cmp_lt_u32 s31, 64
	global_load_lds_dwordx4 v[2:3], off
	s_cselect_b64 s[22:23], -1, 0
	s_cmpk_lt_u32 s31, 0x100
	v_readlane_b32 s36, v252, 29
	s_cselect_b64 s[24:25], -1, 0
	s_and_b32 s0, s30, 7
	s_ashr_i32 s1, s59, 3
	v_readlane_b32 s37, v252, 30
	s_mul_i32 s0, s1, s0
	s_ashr_i32 s1, s30, 3
	v_readlane_b32 s38, v252, 31
	v_readlane_b32 s39, v252, 32
	s_and_b32 s37, s66, 0xffff
	v_or_b32_e32 v178, s2, v11
	s_add_i32 s2, s0, s1
	s_lshl_b64 s[26:27], s[26:27], 2
	v_writelane_b32 v252, s36, 29
	s_waitcnt vmcnt(6)
	s_and_b64 s[0:1], s[28:29], exec
	s_cselect_b32 s78, s2, s30
	v_writelane_b32 v252, s37, 30
	v_writelane_b32 v252, s38, 31
	v_mov_b32_e32 v2, 0
	v_or_b32_e32 v179, 0xfffff800, v178
	s_mov_b32 s81, 0
	v_cmp_ne_u32_e64 s[6:7], 0, v0
	v_writelane_b32 v252, s39, 32
	s_ashr_i32 s79, s78, 31
	s_mov_b32 s50, -1
	v_add_u32_e32 v180, 0, v13
	v_mov_b32_e32 v3, v2
	v_mov_b32_e32 v4, v2
	v_mov_b32_e32 v5, v2
	v_mov_b32_e32 v6, v2
	v_mov_b32_e32 v7, v2
	v_mov_b32_e32 v8, v2
	v_mov_b32_e32 v9, v2
	v_mov_b32_e32 v10, v2
	v_mov_b32_e32 v11, v2
	v_mov_b32_e32 v12, v2
	v_mov_b32_e32 v13, v2
	v_mov_b32_e32 v14, v2
	v_mov_b32_e32 v15, v2
	v_mov_b32_e32 v16, v2
	v_mov_b32_e32 v17, v2
	v_mov_b32_e32 v18, v2
	v_mov_b32_e32 v19, v2
	v_mov_b32_e32 v20, v2
	v_mov_b32_e32 v21, v2
	v_mov_b32_e32 v22, v2
	v_mov_b32_e32 v23, v2
	v_mov_b32_e32 v24, v2
	v_mov_b32_e32 v25, v2
	v_mov_b32_e32 v26, v2
	v_mov_b32_e32 v27, v2
	v_mov_b32_e32 v28, v2
	v_mov_b32_e32 v29, v2
	v_mov_b32_e32 v30, v2
	v_mov_b32_e32 v31, v2
	v_mov_b32_e32 v32, v2
	v_mov_b32_e32 v33, v2
	v_mov_b32_e32 v38, v2
	v_mov_b32_e32 v39, v2
	v_mov_b32_e32 v40, v2
	v_mov_b32_e32 v41, v2
	v_mov_b32_e32 v42, v2
	v_mov_b32_e32 v43, v2
	v_mov_b32_e32 v44, v2
	v_mov_b32_e32 v45, v2
	v_mov_b32_e32 v46, v2
	v_mov_b32_e32 v47, v2
	v_mov_b32_e32 v48, v2
	v_mov_b32_e32 v49, v2
	v_mov_b32_e32 v50, v2
	v_mov_b32_e32 v51, v2
	v_mov_b32_e32 v52, v2
	v_mov_b32_e32 v53, v2
	v_mov_b32_e32 v54, v2
	v_mov_b32_e32 v55, v2
	v_mov_b32_e32 v56, v2
	v_mov_b32_e32 v57, v2
	v_mov_b32_e32 v58, v2
	v_mov_b32_e32 v59, v2
	v_mov_b32_e32 v60, v2
	v_mov_b32_e32 v61, v2
	v_mov_b32_e32 v62, v2
	v_mov_b32_e32 v63, v2
	v_mov_b32_e32 v64, v2
	v_mov_b32_e32 v65, v2
	v_mov_b32_e32 v66, v2
	v_mov_b32_e32 v67, v2
	v_mov_b32_e32 v68, v2
	v_mov_b32_e32 v69, v2
	v_mov_b32_e32 v70, v2
	v_mov_b32_e32 v71, v2
	v_mov_b32_e32 v72, v2
	v_mov_b32_e32 v73, v2
	v_mov_b32_e32 v74, v2
	v_mov_b32_e32 v75, v2
	v_mov_b32_e32 v76, v2
	v_mov_b32_e32 v77, v2
	v_mov_b32_e32 v78, v2
	v_mov_b32_e32 v79, v2
	v_mov_b32_e32 v80, v2
	v_mov_b32_e32 v81, v2
	v_mov_b32_e32 v82, v2
	v_mov_b32_e32 v83, v2
	v_mov_b32_e32 v84, v2
	v_mov_b32_e32 v85, v2
	v_mov_b32_e32 v86, v2
	v_mov_b32_e32 v87, v2
	v_mov_b32_e32 v88, v2
	v_mov_b32_e32 v89, v2
	v_mov_b32_e32 v90, v2
	v_mov_b32_e32 v91, v2
	v_mov_b32_e32 v92, v2
	v_mov_b32_e32 v93, v2
	v_mov_b32_e32 v94, v2
	v_mov_b32_e32 v95, v2
	v_mov_b32_e32 v96, v2
	v_mov_b32_e32 v97, v2
	v_mov_b32_e32 v98, v2
	v_mov_b32_e32 v99, v2
	v_mov_b32_e32 v100, v2
	v_mov_b32_e32 v101, v2
	v_mov_b32_e32 v102, v2
	v_mov_b32_e32 v103, v2
	v_mov_b32_e32 v104, v2
	v_mov_b32_e32 v105, v2
	v_mov_b32_e32 v106, v2
	v_mov_b32_e32 v107, v2
	v_mov_b32_e32 v108, v2
	v_mov_b32_e32 v109, v2
	v_mov_b32_e32 v110, v2
	v_mov_b32_e32 v111, v2
	v_mov_b32_e32 v112, v2
	v_mov_b32_e32 v113, v2
	v_mov_b32_e32 v114, v2
	v_mov_b32_e32 v115, v2
	v_mov_b32_e32 v116, v2
	v_mov_b32_e32 v117, v2
	v_mov_b32_e32 v118, v2
	v_mov_b32_e32 v119, v2
	v_mov_b32_e32 v120, v2
	v_mov_b32_e32 v121, v2
	v_mov_b32_e32 v122, v2
	v_mov_b32_e32 v123, v2
	v_mov_b32_e32 v124, v2
	v_mov_b32_e32 v125, v2
	v_mov_b32_e32 v126, v2
	v_mov_b32_e32 v127, v2
	v_mov_b32_e32 v128, v2
	v_mov_b32_e32 v129, v2
	v_mov_b32_e32 v130, v2
	v_mov_b32_e32 v131, v2
	v_mov_b32_e32 v132, v2
	v_mov_b32_e32 v133, v2
	s_barrier
	s_mov_b32 s32, 0
	s_mov_b32 s98, 0

.LBB0_2042:
	v_cndmask_b32_e64 v0, 0, 1, s[42:43]
	v_cmp_ne_u32_e64 s[0:1], 1, v0
	s_andn2_b64 vcc, exec, s[42:43]
	v_mov_b32_e32 v187, v160
	v_mov_b32_e32 v181, v154
	v_mov_b32_e32 v186, v156
	v_mov_b32_e32 v188, v158
	v_lshrrev_b32_e32 v223, 11, v160
	v_lshrrev_b32_e32 v250, 11, v154
	v_lshrrev_b32_e32 v249, 11, v156
	v_lshrrev_b32_e32 v248, 11, v158
	s_cbranch_vccnz .LBB0_2060
	s_andn2_b64 vcc, exec, s[2:3]
	s_cbranch_vccnz .LBB0_2054
	s_andn2_b64 vcc, exec, s[22:23]
	s_cbranch_vccnz .LBB0_2053
	s_ashr_i32 s31, s30, 31
	s_lshl_b64 s[2:3], s[30:31], 2
	s_add_u32 s2, s14, s2
	s_addc_u32 s3, s15, s3
	s_add_i32 s29, s30, 1
	s_cmp_lg_u32 s29, s98
	s_cbranch_scc1 .Lep_nopre
	v_readfirstlane_b32 s29, v190
	s_cmp_gt_u32 s29, 7
	s_cbranch_scc1 .LBB0_2052
.Lep_nopre:
	s_mov_b32 s13, 0x1000001
	s_branch .LBB0_2047

.LBB0_2067:
	s_mov_b32 s98, 0
	s_andn2_b64 vcc, exec, s[22:23]
	s_cbranch_vccnz .Lep_skip
	s_add_i32 s99, s82, 1
	s_mul_i32 s99, s99, s59
	s_add_i32 s99, s99, s78
	s_sub_i32 s99, s99, s8
	s_cmp_lt_i32 s99, 0
	s_cbranch_scc1 .Lep_skip
	s_cmp_ge_i32 s99, s26
	s_cbranch_scc1 .Lep_skip
	s_lshr_b32 s99, s99, 2
	s_add_i32 s98, s99, 1
	s_lshl_b32 s99, s99, 2
	v_mov_b32_e32 v190, s99
	s_nop 0
	global_load_dword v190, v190, s[14:15] sc1
